# speedup vs baseline: 1.0057x; 1.0057x over previous
.Lattn_A:
	ds_read_b128 v[34:37], v114
	ds_read_b128 v[42:45], v114 offset:4096
	s_add_i32 s48, s66, s64
	s_cmp_lg_u32 s48, 1
	s_waitcnt lgkmcnt(1)
	v_mfma_f32_16x16x32_f16 v[34:37], v[34:37], v[6:9], v[30:33]
	ds_read_b128 v[38:41], v114 offset:2048
	ds_read_b128 v[46:49], v114 offset:6144
	s_waitcnt lgkmcnt(2)
	v_mfma_f32_16x16x32_f16 v[102:105], v[42:45], v[6:9], v[30:33]
	ds_read_b128 v[42:45], v115
	ds_read_b128 v[110:113], v115 offset:2048
	s_waitcnt lgkmcnt(3)
	v_mfma_f32_16x16x32_f16 v[38:41], v[38:41], v[6:9], v[30:33]
	s_waitcnt lgkmcnt(2)
	v_mfma_f32_16x16x32_f16 v[106:109], v[46:49], v[6:9], v[30:33]
	s_waitcnt lgkmcnt(1)
	v_mfma_f32_16x16x32_f16 v[46:49], v[42:45], v[2:5], v[34:37]
	s_nop 2
	ds_read_b128 v[34:37], v115 offset:4096
	s_waitcnt lgkmcnt(1)
	v_mfma_f32_16x16x32_f16 v[42:45], v[110:113], v[2:5], v[38:41]
	ds_read_b128 v[110:113], v115 offset:6144
	s_waitcnt lgkmcnt(1)
	v_mfma_f32_16x16x32_f16 v[38:41], v[34:37], v[2:5], v[102:105]
	s_waitcnt lgkmcnt(0)
	v_mfma_f32_16x16x32_f16 v[34:37], v[110:113], v[2:5], v[106:109]
	s_cbranch_scc1 .LBB2_12
	v_cndmask_b32_e64 v69, v46, v100, s[2:3]
	v_cndmask_b32_e64 v46, v69, v46, s[4:5]
	v_cndmask_b32_e64 v47, v100, v47, s[4:5]
	v_cndmask_b32_e64 v48, v48, v100, s[6:7]
	v_cndmask_b32_e64 v49, v49, v100, s[8:9]
	v_cndmask_b32_e64 v42, v42, v100, s[10:11]
	v_cndmask_b32_e64 v43, v43, v100, s[12:13]
	v_cndmask_b32_e64 v44, v44, v100, s[14:15]
	v_cndmask_b32_e64 v45, v45, v100, s[16:17]
	v_cndmask_b32_e64 v38, v38, v100, s[18:19]
	v_cndmask_b32_e64 v39, v39, v100, s[20:21]
	v_cndmask_b32_e64 v40, v40, v100, s[22:23]
	v_cndmask_b32_e64 v41, v41, v100, s[24:25]
	v_cndmask_b32_e64 v34, v34, v100, s[26:27]
	v_cndmask_b32_e64 v35, v35, v100, s[28:29]
	v_cndmask_b32_e64 v36, v36, v100, s[30:31]
	v_cndmask_b32_e64 v37, v37, v100, s[34:35]
